# v49 + same loop-edge edit in the WO and M1 K-loops (fragment reads ahead of the scalar address block at the back edge)
# baseline (speedup 1.0000x reference)
.LBB0_969:
	s_waitcnt lgkmcnt(0)
	v_add_u32_e32 v104, 0x10000, v234
	ds_read_b128 v[162:165], v104
	ds_read_b128 v[166:169], v104 offset:1024
	ds_read_b128 v[170:173], v104 offset:2048
	ds_read_b128 v[174:177], v104 offset:3072
	v_add_u32_e32 v104, 0x14000, v234
	ds_read_b128 v[146:149], v104
	ds_read_b128 v[150:153], v104 offset:1024
	ds_read_b128 v[154:157], v104 offset:2048
	ds_read_b128 v[158:161], v104 offset:3072
	ds_read_b128 v[178:181], v236
	ds_read_b128 v[182:185], v236 offset:1024
	ds_read_b128 v[186:189], v236 offset:2048
	ds_read_b128 v[190:193], v236 offset:3072
	ds_read_b128 v[210:213], v236 offset:4096
	ds_read_b128 v[214:217], v236 offset:5120
	ds_read_b128 v[218:221], v236 offset:6144
	ds_read_b128 v[222:225], v236 offset:7168
	s_add_u32 s24, s18, s92
	s_addc_u32 s25, s19, s93
	s_add_u32 s60, s24, 0x100
	s_addc_u32 s61, s25, 0
	s_add_u32 s81, s2, s92
	s_addc_u32 s84, s29, s93
	s_add_i32 vcc_lo, 0, 0x10000
	s_cmpk_eq_i32 s92, 0xf00
	s_cselect_b64 s[26:27], -1, 0
	s_and_b64 s[24:25], s[26:27], exec
	s_cselect_b32 s25, s15, s61
	s_cselect_b32 s24, s17, s60
	s_cselect_b32 s85, s67, s84
	s_cselect_b32 s84, s3, s81
	s_add_i32 s81, 0, 0x14000
	v_lshl_add_u64 v[104:105], v[208:209], 0, s[92:93]
	s_add_i32 m0, s53, 0xc000
	s_nop 0
	global_load_lds_dwordx4 v[104:105], off
	v_lshl_add_u64 v[104:105], v[206:207], 0, s[92:93]
	s_add_i32 m0, s53, 0xe000
	s_nop 0
	global_load_lds_dwordx4 v[104:105], off
	s_waitcnt vmcnt(8)
	s_waitcnt lgkmcnt(0)
	s_barrier
	v_mfma_f32_16x16x32_bf16 v[104:107], v[162:165], v[178:181], v[142:145]
	v_mfma_f32_16x16x32_bf16 v[108:111], v[170:173], v[178:181], v[138:141]
	v_mfma_f32_16x16x32_bf16 v[116:119], v[162:165], v[186:189], v[120:123]
	v_mfma_f32_16x16x32_bf16 v[112:115], v[170:173], v[186:189], v[112:115]
	v_mfma_f32_16x16x32_bf16 v[92:95], v[162:165], v[210:213], v[92:95]
	v_mfma_f32_16x16x32_bf16 v[88:91], v[170:173], v[210:213], v[88:91]
	v_mfma_f32_16x16x32_bf16 v[76:79], v[162:165], v[218:221], v[76:79]
	v_mfma_f32_16x16x32_bf16 v[72:75], v[170:173], v[218:221], v[72:75]
	v_mfma_f32_16x16x32_bf16 v[104:107], v[166:169], v[182:185], v[104:107]
	v_mfma_f32_16x16x32_bf16 v[108:111], v[174:177], v[182:185], v[108:111]
	v_mfma_f32_16x16x32_bf16 v[116:119], v[166:169], v[190:193], v[116:119]
	v_mfma_f32_16x16x32_bf16 v[112:115], v[174:177], v[190:193], v[112:115]
	v_mfma_f32_16x16x32_bf16 v[92:95], v[166:169], v[214:217], v[92:95]
	v_mfma_f32_16x16x32_bf16 v[88:91], v[174:177], v[214:217], v[88:91]
	v_mfma_f32_16x16x32_bf16 v[76:79], v[166:169], v[222:225], v[76:79]
	v_mfma_f32_16x16x32_bf16 v[72:75], v[174:177], v[222:225], v[72:75]
	v_mfma_f32_16x16x32_bf16 v[120:123], v[146:149], v[178:181], v[134:137]
	v_mfma_f32_16x16x32_bf16 v[130:133], v[150:153], v[182:185], v[120:123]
	v_mfma_f32_16x16x32_bf16 v[120:123], v[154:157], v[178:181], v[124:127]
	v_mfma_f32_16x16x32_bf16 v[100:103], v[146:149], v[186:189], v[100:103]
	v_mfma_f32_16x16x32_bf16 v[96:99], v[154:157], v[186:189], v[96:99]
	v_mfma_f32_16x16x32_bf16 v[84:87], v[146:149], v[210:213], v[84:87]
	v_mfma_f32_16x16x32_bf16 v[80:83], v[154:157], v[210:213], v[80:83]
	v_mfma_f32_16x16x32_bf16 v[68:71], v[146:149], v[218:221], v[68:71]
	v_mfma_f32_16x16x32_bf16 v[64:67], v[154:157], v[218:221], v[64:67]
	v_mfma_f32_16x16x32_bf16 v[124:127], v[158:161], v[182:185], v[120:123]
	v_mfma_f32_16x16x32_bf16 v[100:103], v[150:153], v[190:193], v[100:103]
	v_mfma_f32_16x16x32_bf16 v[96:99], v[158:161], v[190:193], v[96:99]
	v_mfma_f32_16x16x32_bf16 v[84:87], v[150:153], v[214:217], v[84:87]
	v_mfma_f32_16x16x32_bf16 v[80:83], v[158:161], v[214:217], v[80:83]
	v_mfma_f32_16x16x32_bf16 v[68:71], v[150:153], v[222:225], v[68:71]
	v_mfma_f32_16x16x32_bf16 v[64:67], v[158:161], v[222:225], v[64:67]
	s_barrier
	s_add_i32 s60, vcc_lo, s39
	v_lshl_add_u64 v[210:211], s[84:85], 0, v[198:199]
	s_mov_b32 m0, s60
	ds_read_b128 v[186:189], v236 offset:16384
	ds_read_b128 v[190:193], v236 offset:17408
	ds_read_b128 v[178:181], v236 offset:18432
	ds_read_b128 v[182:185], v236 offset:19456
	ds_read_b128 v[138:141], v236 offset:20480
	ds_read_b128 v[142:145], v236 offset:21504
	ds_read_b128 v[120:123], v236 offset:22528
	ds_read_b128 v[134:137], v236 offset:23552
	global_load_lds_dwordx4 v[210:211], off
	s_add_i32 m0, s60, 0x2000
	s_add_u32 s60, s84, 0x80000
	v_lshl_add_u64 v[212:213], s[84:85], 0, v[200:201]
	s_addc_u32 s61, s85, 0
	s_add_i32 s81, s81, s39
	global_load_lds_dwordx4 v[212:213], off
	v_lshl_add_u64 v[214:215], s[60:61], 0, v[198:199]
	s_mov_b32 m0, s81
	v_lshl_add_u64 v[216:217], s[24:25], 0, v[200:201]
	global_load_lds_dwordx4 v[214:215], off
	v_lshl_add_u64 v[214:215], s[60:61], 0, v[200:201]
	s_add_i32 m0, s81, 0x2000
	v_cndmask_b32_e64 v128, 0, 1, s[96:97]
	global_load_lds_dwordx4 v[214:215], off
	v_lshl_add_u64 v[214:215], s[24:25], 0, v[198:199]
	s_mov_b32 m0, s53
	v_cmp_ne_u32_e64 s[60:61], 1, v128
	global_load_lds_dwordx4 v[214:215], off
	s_mov_b32 m0, s88
	s_andn2_b64 vcc, exec, s[96:97]
	global_load_lds_dwordx4 v[216:217], off
	s_waitcnt vmcnt(8)
	s_waitcnt lgkmcnt(0)
	s_barrier
	s_cbranch_vccnz .LBB0_971
	s_waitcnt lgkmcnt(0)
	v_mfma_f32_16x16x32_bf16 v[60:63], v[162:165], v[186:189], v[60:63]
	v_mfma_f32_16x16x32_bf16 v[56:59], v[170:173], v[186:189], v[56:59]
	v_mfma_f32_16x16x32_bf16 v[44:47], v[162:165], v[178:181], v[44:47]
	v_mfma_f32_16x16x32_bf16 v[40:43], v[170:173], v[178:181], v[40:43]
	v_mfma_f32_16x16x32_bf16 v[28:31], v[162:165], v[138:141], v[28:31]
	v_mfma_f32_16x16x32_bf16 v[24:27], v[170:173], v[138:141], v[24:27]
	v_mfma_f32_16x16x32_bf16 v[12:15], v[162:165], v[120:123], v[12:15]
	v_mfma_f32_16x16x32_bf16 v[8:11], v[170:173], v[120:123], v[8:11]
	v_mfma_f32_16x16x32_bf16 v[60:63], v[166:169], v[190:193], v[60:63]
	v_mfma_f32_16x16x32_bf16 v[56:59], v[174:177], v[190:193], v[56:59]
	v_mfma_f32_16x16x32_bf16 v[44:47], v[166:169], v[182:185], v[44:47]
	v_mfma_f32_16x16x32_bf16 v[40:43], v[174:177], v[182:185], v[40:43]
	v_mfma_f32_16x16x32_bf16 v[28:31], v[166:169], v[142:145], v[28:31]
	v_mfma_f32_16x16x32_bf16 v[24:27], v[174:177], v[142:145], v[24:27]
	v_mfma_f32_16x16x32_bf16 v[12:15], v[166:169], v[134:137], v[12:15]
	v_mfma_f32_16x16x32_bf16 v[8:11], v[174:177], v[134:137], v[8:11]
	v_mfma_f32_16x16x32_bf16 v[52:55], v[146:149], v[186:189], v[52:55]
	v_mfma_f32_16x16x32_bf16 v[48:51], v[154:157], v[186:189], v[48:51]
	v_mfma_f32_16x16x32_bf16 v[36:39], v[146:149], v[178:181], v[36:39]
	v_mfma_f32_16x16x32_bf16 v[32:35], v[154:157], v[178:181], v[32:35]
	v_mfma_f32_16x16x32_bf16 v[20:23], v[146:149], v[138:141], v[20:23]
	v_mfma_f32_16x16x32_bf16 v[16:19], v[154:157], v[138:141], v[16:19]
	v_mfma_f32_16x16x32_bf16 v[4:7], v[146:149], v[120:123], v[4:7]
	v_mfma_f32_16x16x32_bf16 v[0:3], v[154:157], v[120:123], v[0:3]
	v_mfma_f32_16x16x32_bf16 v[52:55], v[150:153], v[190:193], v[52:55]
	v_mfma_f32_16x16x32_bf16 v[48:51], v[158:161], v[190:193], v[48:51]
	v_mfma_f32_16x16x32_bf16 v[36:39], v[150:153], v[182:185], v[36:39]
	v_mfma_f32_16x16x32_bf16 v[32:35], v[158:161], v[182:185], v[32:35]
	v_mfma_f32_16x16x32_bf16 v[20:23], v[150:153], v[142:145], v[20:23]
	v_mfma_f32_16x16x32_bf16 v[16:19], v[158:161], v[142:145], v[16:19]
	v_mfma_f32_16x16x32_bf16 v[4:7], v[150:153], v[134:137], v[4:7]
	v_mfma_f32_16x16x32_bf16 v[0:3], v[158:161], v[134:137], v[0:3]

.LBB0_1400:
	v_add_u32_e32 v128, s26, v242
	ds_read_b128 v[130:133], v128
	ds_read_b128 v[134:137], v128 offset:1024
	ds_read_b128 v[138:141], v128 offset:2048
	ds_read_b128 v[142:145], v128 offset:3072
	v_add_u32_e32 v128, 0x14000, v242
	ds_read_b128 v[146:149], v128
	ds_read_b128 v[150:153], v128 offset:1024
	ds_read_b128 v[154:157], v128 offset:2048
	ds_read_b128 v[158:161], v128 offset:3072
	ds_read_b128 v[162:165], v209
	ds_read_b128 v[166:169], v209 offset:1024
	ds_read_b128 v[170:173], v209 offset:2048
	ds_read_b128 v[174:177], v209 offset:3072
	ds_read_b128 v[178:181], v209 offset:4096
	ds_read_b128 v[182:185], v209 offset:5120
	ds_read_b128 v[186:189], v209 offset:6144
	ds_read_b128 v[190:193], v209 offset:7168
	s_add_u32 s2, s64, s74
	s_addc_u32 s3, s65, s75
	s_add_u32 s22, s2, 0x28c00100
	s_addc_u32 s23, s3, 0
	s_cmpk_eq_i32 s74, 0xf00
	s_cselect_b64 s[60:61], -1, 0
	s_and_b64 s[2:3], s[60:61], exec
	s_cselect_b32 s23, s9, s23
	s_cselect_b32 s22, s8, s22
	s_add_i32 s2, 0, 0x14000
	v_lshl_add_u64 v[194:195], v[220:221], 0, s[74:75]
	v_cndmask_b32_e64 v223, v195, v207, s[60:61]
	v_cndmask_b32_e64 v222, v194, v206, s[60:61]
	v_lshl_add_u64 v[194:195], v[218:219], 0, s[74:75]
	s_add_i32 m0, s36, 0xc000
	s_nop 0
	global_load_lds_dwordx4 v[194:195], off
	v_lshl_add_u64 v[194:195], v[216:217], 0, s[74:75]
	s_add_i32 m0, s36, 0xe000
	s_nop 0
	global_load_lds_dwordx4 v[194:195], off
	s_waitcnt vmcnt(8)
	s_waitcnt lgkmcnt(0)
	s_barrier
	v_mfma_f32_16x16x32_bf16 v[124:127], v[130:133], v[162:165], v[124:127]
	v_mfma_f32_16x16x32_bf16 v[120:123], v[138:141], v[162:165], v[120:123]
	v_mfma_f32_16x16x32_bf16 v[108:111], v[130:133], v[170:173], v[108:111]
	v_mfma_f32_16x16x32_bf16 v[104:107], v[138:141], v[170:173], v[104:107]
	v_mfma_f32_16x16x32_bf16 v[92:95], v[130:133], v[178:181], v[92:95]
	v_mfma_f32_16x16x32_bf16 v[88:91], v[138:141], v[178:181], v[88:91]
	v_mfma_f32_16x16x32_bf16 v[76:79], v[130:133], v[186:189], v[76:79]
	v_mfma_f32_16x16x32_bf16 v[72:75], v[138:141], v[186:189], v[72:75]
	v_mfma_f32_16x16x32_bf16 v[124:127], v[134:137], v[166:169], v[124:127]
	v_mfma_f32_16x16x32_bf16 v[120:123], v[142:145], v[166:169], v[120:123]
	v_mfma_f32_16x16x32_bf16 v[108:111], v[134:137], v[174:177], v[108:111]
	v_mfma_f32_16x16x32_bf16 v[104:107], v[142:145], v[174:177], v[104:107]
	v_mfma_f32_16x16x32_bf16 v[92:95], v[134:137], v[182:185], v[92:95]
	v_mfma_f32_16x16x32_bf16 v[88:91], v[142:145], v[182:185], v[88:91]
	v_mfma_f32_16x16x32_bf16 v[76:79], v[134:137], v[190:193], v[76:79]
	v_mfma_f32_16x16x32_bf16 v[72:75], v[142:145], v[190:193], v[72:75]
	v_mfma_f32_16x16x32_bf16 v[116:119], v[146:149], v[162:165], v[116:119]
	v_mfma_f32_16x16x32_bf16 v[112:115], v[154:157], v[162:165], v[112:115]
	v_mfma_f32_16x16x32_bf16 v[100:103], v[146:149], v[170:173], v[100:103]
	v_mfma_f32_16x16x32_bf16 v[96:99], v[154:157], v[170:173], v[96:99]
	v_mfma_f32_16x16x32_bf16 v[84:87], v[146:149], v[178:181], v[84:87]
	v_mfma_f32_16x16x32_bf16 v[80:83], v[154:157], v[178:181], v[80:83]
	v_mfma_f32_16x16x32_bf16 v[68:71], v[146:149], v[186:189], v[68:71]
	v_mfma_f32_16x16x32_bf16 v[64:67], v[154:157], v[186:189], v[64:67]
	v_mfma_f32_16x16x32_bf16 v[116:119], v[150:153], v[166:169], v[116:119]
	v_mfma_f32_16x16x32_bf16 v[112:115], v[158:161], v[166:169], v[112:115]
	v_mfma_f32_16x16x32_bf16 v[100:103], v[150:153], v[174:177], v[100:103]
	v_mfma_f32_16x16x32_bf16 v[96:99], v[158:161], v[174:177], v[96:99]
	v_mfma_f32_16x16x32_bf16 v[84:87], v[150:153], v[182:185], v[84:87]
	v_mfma_f32_16x16x32_bf16 v[80:83], v[158:161], v[182:185], v[80:83]
	v_mfma_f32_16x16x32_bf16 v[68:71], v[150:153], v[190:193], v[68:71]
	v_mfma_f32_16x16x32_bf16 v[64:67], v[158:161], v[190:193], v[64:67]
	s_barrier
	s_add_i32 s3, s26, s33
	v_lshl_add_u64 v[224:225], v[222:223], 0, v[198:199]
	s_mov_b32 m0, s3
	ds_read_b128 v[186:189], v209 offset:16384
	ds_read_b128 v[190:193], v209 offset:17408
	ds_read_b128 v[178:181], v209 offset:18432
	ds_read_b128 v[182:185], v209 offset:19456
	ds_read_b128 v[170:173], v209 offset:20480
	ds_read_b128 v[174:177], v209 offset:21504
	ds_read_b128 v[162:165], v209 offset:22528
	ds_read_b128 v[166:169], v209 offset:23552
	global_load_lds_dwordx4 v[224:225], off
	v_lshl_add_u64 v[226:227], v[222:223], 0, v[200:201]
	s_add_i32 m0, s3, 0x2000
	v_lshl_add_u64 v[194:195], v[222:223], 0, s[40:41]
	s_add_i32 s2, s2, s33
	global_load_lds_dwordx4 v[226:227], off
	v_lshl_add_u64 v[196:197], v[194:195], 0, v[198:199]
	s_mov_b32 m0, s2
	v_lshl_add_u64 v[194:195], v[194:195], 0, v[200:201]
	global_load_lds_dwordx4 v[196:197], off
	s_add_i32 m0, s2, 0x2000
	v_cndmask_b32_e64 v128, v208, v211, s[60:61]
	global_load_lds_dwordx4 v[194:195], off
	s_mov_b32 m0, s36
	v_cndmask_b32_e64 v228, v210, v243, s[60:61]
	global_load_lds_dwordx4 v128, s[22:23]
	s_mov_b32 m0, s37
	v_cndmask_b32_e64 v194, 0, 1, s[20:21]
	global_load_lds_dwordx4 v228, s[22:23]
	s_waitcnt vmcnt(8)
	s_waitcnt lgkmcnt(0)
	v_cmp_ne_u32_e64 s[62:63], 1, v194
	s_andn2_b64 vcc, exec, s[20:21]
	s_barrier
	s_cbranch_vccnz .LBB0_1402
	s_waitcnt lgkmcnt(0)
	v_mfma_f32_16x16x32_bf16 v[60:63], v[130:133], v[186:189], v[60:63]
	v_mfma_f32_16x16x32_bf16 v[56:59], v[138:141], v[186:189], v[56:59]
	v_mfma_f32_16x16x32_bf16 v[44:47], v[130:133], v[178:181], v[44:47]
	v_mfma_f32_16x16x32_bf16 v[40:43], v[138:141], v[178:181], v[40:43]
	v_mfma_f32_16x16x32_bf16 v[28:31], v[130:133], v[170:173], v[28:31]
	v_mfma_f32_16x16x32_bf16 v[24:27], v[138:141], v[170:173], v[24:27]
	v_mfma_f32_16x16x32_bf16 v[12:15], v[130:133], v[162:165], v[12:15]
	v_mfma_f32_16x16x32_bf16 v[8:11], v[138:141], v[162:165], v[8:11]
	v_mfma_f32_16x16x32_bf16 v[60:63], v[134:137], v[190:193], v[60:63]
	v_mfma_f32_16x16x32_bf16 v[56:59], v[142:145], v[190:193], v[56:59]
	v_mfma_f32_16x16x32_bf16 v[44:47], v[134:137], v[182:185], v[44:47]
	v_mfma_f32_16x16x32_bf16 v[40:43], v[142:145], v[182:185], v[40:43]
	v_mfma_f32_16x16x32_bf16 v[28:31], v[134:137], v[174:177], v[28:31]
	v_mfma_f32_16x16x32_bf16 v[24:27], v[142:145], v[174:177], v[24:27]
	v_mfma_f32_16x16x32_bf16 v[12:15], v[134:137], v[166:169], v[12:15]
	v_mfma_f32_16x16x32_bf16 v[8:11], v[142:145], v[166:169], v[8:11]
	v_mfma_f32_16x16x32_bf16 v[52:55], v[146:149], v[186:189], v[52:55]
	v_mfma_f32_16x16x32_bf16 v[48:51], v[154:157], v[186:189], v[48:51]
	v_mfma_f32_16x16x32_bf16 v[36:39], v[146:149], v[178:181], v[36:39]
	v_mfma_f32_16x16x32_bf16 v[32:35], v[154:157], v[178:181], v[32:35]
	v_mfma_f32_16x16x32_bf16 v[20:23], v[146:149], v[170:173], v[20:23]
	v_mfma_f32_16x16x32_bf16 v[16:19], v[154:157], v[170:173], v[16:19]
	v_mfma_f32_16x16x32_bf16 v[4:7], v[146:149], v[162:165], v[4:7]
	v_mfma_f32_16x16x32_bf16 v[0:3], v[154:157], v[162:165], v[0:3]
	v_mfma_f32_16x16x32_bf16 v[52:55], v[150:153], v[190:193], v[52:55]
	v_mfma_f32_16x16x32_bf16 v[48:51], v[158:161], v[190:193], v[48:51]
	v_mfma_f32_16x16x32_bf16 v[36:39], v[150:153], v[182:185], v[36:39]
	v_mfma_f32_16x16x32_bf16 v[32:35], v[158:161], v[182:185], v[32:35]
	v_mfma_f32_16x16x32_bf16 v[20:23], v[150:153], v[174:177], v[20:23]
	v_mfma_f32_16x16x32_bf16 v[16:19], v[158:161], v[174:177], v[16:19]
	v_mfma_f32_16x16x32_bf16 v[4:7], v[150:153], v[166:169], v[4:7]
	v_mfma_f32_16x16x32_bf16 v[0:3], v[158:161], v[166:169], v[0:3]
